# v71 + MLA max-subtraction v_subs spread 4-6 per PV MFMA gap instead of 8 in the last four gaps
# speedup vs baseline: 1.0077x; 1.0077x over previous
.Lmla_pv_mfma:
	s_waitcnt lgkmcnt(4)
	s_nop 0
	v_mfma_f32_32x32x16_bf16 v[18:33], v[90:93], v[126:129], v[18:33]
	v_mfma_f32_32x32x16_bf16 v[2:17], v[90:93], v[130:133], v[2:17]
	v_sub_f32_e32 v65, v65, v123
	v_sub_f32_e32 v64, v64, v123
	v_sub_f32_e32 v63, v63, v123
	v_sub_f32_e32 v62, v62, v123
	ds_read_b64_tr_b16 v[126:127], v125 offset:0x1000
	ds_read_b64_tr_b16 v[128:129], v125 offset:0x1400
	ds_read_b64_tr_b16 v[130:131], v125 offset:0x1200
	ds_read_b64_tr_b16 v[132:133], v125 offset:0x1600
	s_waitcnt lgkmcnt(4)
	v_mfma_f32_32x32x16_bf16 v[18:33], v[94:97], v[134:137], v[18:33]
	v_sub_f32_e32 v61, v61, v123
	v_sub_f32_e32 v60, v60, v123
	v_sub_f32_e32 v59, v59, v123
	v_sub_f32_e32 v58, v58, v123
	v_mfma_f32_32x32x16_bf16 v[2:17], v[94:97], v[138:141], v[2:17]
	v_sub_f32_e32 v57, v57, v123
	v_sub_f32_e32 v56, v56, v123
	v_sub_f32_e32 v55, v55, v123
	v_sub_f32_e32 v54, v54, v123
	ds_read_b64_tr_b16 v[134:135], v125 offset:0x1800
	ds_read_b64_tr_b16 v[136:137], v125 offset:0x1c00
	ds_read_b64_tr_b16 v[138:139], v125 offset:0x1a00
	ds_read_b64_tr_b16 v[140:141], v125 offset:0x1e00
	s_waitcnt lgkmcnt(4)
	v_mfma_f32_32x32x16_bf16 v[18:33], v[98:101], v[126:129], v[18:33]
	v_sub_f32_e32 v53, v53, v123
	v_sub_f32_e32 v52, v52, v123
	v_sub_f32_e32 v51, v51, v123
	v_sub_f32_e32 v50, v50, v123
	v_mfma_f32_32x32x16_bf16 v[2:17], v[98:101], v[130:133], v[2:17]
	v_sub_f32_e32 v49, v49, v123
	v_sub_f32_e32 v48, v48, v123
	v_sub_f32_e32 v47, v47, v123
	v_sub_f32_e32 v46, v46, v123
	v_sub_f32_e32 v45, v45, v123
	s_waitcnt lgkmcnt(0)
	v_mfma_f32_32x32x16_bf16 v[18:33], v[102:105], v[134:137], v[18:33]
	v_sub_f32_e32 v44, v44, v123
	v_sub_f32_e32 v43, v43, v123
	v_sub_f32_e32 v42, v42, v123
	v_sub_f32_e32 v41, v41, v123
	v_sub_f32_e32 v40, v40, v123
	v_mfma_f32_32x32x16_bf16 v[2:17], v[102:105], v[138:141], v[2:17]
	v_sub_f32_e32 v39, v39, v123
	v_sub_f32_e32 v38, v38, v123
	v_sub_f32_e32 v37, v37, v123
	v_sub_f32_e32 v36, v36, v123
	v_sub_f32_e32 v35, v35, v123
	v_sub_f32_e32 v34, v34, v123
